# merge GEMM epilogue: gate bytes of chunks 1-3 prefetched into free fragment registers at the top of the epilogue (counted vmcnt waits + copies) instead of 4 serialized load/wait rounds; plus attention
# speedup vs baseline: 1.0089x; 1.0054x over previous
;     __device__ __forceinline__ void operator()(AccT& acc, const gm::GUnit& u, int wr, int wc, int fr, int fq) const {
;     ...
;         const unsigned char* gbase = G8 + (size_t)(u.pm * 256 + wr * 64 + fr) * INW + k * 1024 + u.pn * 256 + wc * 32 + 8 * fq;
; #pragma unroll
;         for (int q = 0; q < 4; ++q) {
;             const int ai = q >> 1, m0 = (q & 1) * 2;
;             u32x2 ga[2][2], gb[2][2];
; #pragma unroll
;             for (int mi = 0; mi < 2; ++mi)
; #pragma unroll
;                 for (int bj = 0; bj < 2; ++bj) {
;                     const unsigned char* gp = gbase + (size_t)(ai * 128 + (m0 + mi) * 16) * INW + bj * 128;
;                     ga[mi][bj] = *(const u32x2*)gp;
;                     gb[mi][bj] = (k < 3) ? *(const u32x2*)(gp + 1024) : (u32x2){0xffffffffu, 0xffffffffu};
;                 }
;             __builtin_amdgcn_sched_barrier(0);
; #pragma unroll
;             for (int mi = 0; mi < 2; ++mi) {
;                 const int m = m0 + mi, row = u.pm * 256 + ai * 128 + wr * 64 + m * 16 + fr;
; #pragma unroll
;                 for (int bj = 0; bj < 2; ++bj) {
;                     const u32x2 a = ga[mi][bj], b = gb[mi][bj];
;                     f32x4 r0, r1;
;                     r0[0] = (float)(a.x & 255u) * __builtin_amdgcn_rcpf((float)(b.x & 255u)); r0[1] = (float)((a.x >> 8) & 255u) * __builtin_amdgcn_rcpf((float)((b.x >> 8) & 255u));
;                     r0[2] = (float)((a.x >> 16) & 255u) * __builtin_amdgcn_rcpf((float)((b.x >> 16) & 255u)); r0[3] = (float)(a.x >> 24) * __builtin_amdgcn_rcpf((float)(b.x >> 24));
;                     r1[0] = (float)(a.y & 255u) * __builtin_amdgcn_rcpf((float)(b.y & 255u)); r1[1] = (float)((a.y >> 8) & 255u) * __builtin_amdgcn_rcpf((float)((b.y >> 8) & 255u));
;                     r1[2] = (float)((a.y >> 16) & 255u) * __builtin_amdgcn_rcpf((float)((b.y >> 16) & 255u)); r1[3] = (float)(a.y >> 24) * __builtin_amdgcn_rcpf((float)(b.y >> 24));
;                     const f32x4 s0 = acc[ai][bj][m][0] * r0, s1 = acc[ai][bj][m][1] * r1;
;                     if (k == 3) {
;                         u32x4 w; w.x = cvt_pk_bf16(s0[0], s0[1]); w.y = cvt_pk_bf16(s0[2], s0[3]); w.z = cvt_pk_bf16(s1[0], s1[1]); w.w = cvt_pk_bf16(s1[2], s1[3]);
;                         *(u32x4*)(M + (size_t)row * DM + u.pn * 256 + bj * 128 + wc * 32 + 8 * fq) = w;
;                     }
.LBB0_610:
	v_add_co_u32_e32 v234, vcc, 0x20000, v134
	s_nop 1
	v_addc_co_u32_e32 v235, vcc, 0, v135, vcc
	global_load_dwordx2 v[166:167], v[234:235], off
	global_load_dwordx2 v[168:169], v[234:235], off offset:1024
	global_load_dwordx2 v[170:171], v[234:235], off offset:128
	global_load_dwordx2 v[172:173], v[234:235], off offset:1152
	v_add_co_u32_e32 v234, vcc, 0x30000, v134
	s_nop 1
	v_addc_co_u32_e32 v235, vcc, 0, v135, vcc
	global_load_dwordx2 v[174:175], v[234:235], off
	global_load_dwordx2 v[176:177], v[234:235], off offset:1024
	global_load_dwordx2 v[178:179], v[234:235], off offset:128
	global_load_dwordx2 v[192:193], v[234:235], off offset:1152
	v_add_co_u32_e32 v234, vcc, 0x80000, v134
	s_nop 1
	v_addc_co_u32_e32 v235, vcc, 0, v135, vcc
	global_load_dwordx2 v[194:195], v[234:235], off
	global_load_dwordx2 v[200:201], v[234:235], off offset:1024
	global_load_dwordx2 v[202:203], v[234:235], off offset:128
	global_load_dwordx2 v[204:205], v[234:235], off offset:1152
	v_add_co_u32_e32 v234, vcc, 0x90000, v134
	s_nop 1
	v_addc_co_u32_e32 v235, vcc, 0, v135, vcc
	global_load_dwordx2 v[206:207], v[234:235], off
	global_load_dwordx2 v[208:209], v[234:235], off offset:1024
	global_load_dwordx2 v[210:211], v[234:235], off offset:128
	global_load_dwordx2 v[224:225], v[234:235], off offset:1152
	s_cmp_eq_u32 s64, 3
	s_cselect_b64 s[8:9], -1, 0
	s_cmp_lg_u32 s64, 3
	v_lshlrev_b64 v[150:151], 11, v[132:133]
	s_waitcnt vmcnt(16)
	v_cvt_f32_ubyte0_e32 v133, v154
	v_rcp_iflag_f32_e32 v156, v133
	v_cvt_f32_ubyte1_e32 v133, v154
	v_rcp_iflag_f32_e32 v157, v133
	v_cvt_f32_ubyte2_e32 v133, v154
	v_rcp_iflag_f32_e32 v158, v133
	v_cvt_f32_ubyte3_e32 v133, v154
	v_rcp_iflag_f32_e32 v159, v133
	v_cvt_f32_ubyte3_e32 v161, v152
	v_cvt_f32_ubyte2_e32 v160, v152
	v_cvt_f32_ubyte0_e32 v133, v155
	v_pk_mul_f32 v[158:159], v[158:159], v[160:161]
	v_rcp_iflag_f32_e32 v160, v133
	v_cvt_f32_ubyte1_e32 v133, v155
	v_rcp_iflag_f32_e32 v161, v133
	v_cvt_f32_ubyte2_e32 v133, v155
	v_rcp_iflag_f32_e32 v154, v133
	v_cvt_f32_ubyte3_e32 v133, v155
	v_rcp_iflag_f32_e32 v155, v133
	v_cvt_f32_ubyte1_e32 v163, v152
	v_cvt_f32_ubyte0_e32 v162, v152
	v_pk_mul_f32 v[156:157], v[156:157], v[162:163]
	v_cvt_f32_ubyte3_e32 v163, v153
	v_cvt_f32_ubyte2_e32 v162, v153
	v_cvt_f32_ubyte1_e32 v165, v153
	v_cvt_f32_ubyte0_e32 v164, v153
	v_pk_mul_f32 v[152:153], v[160:161], v[164:165]
	v_pk_mul_f32 v[154:155], v[154:155], v[162:163]
	v_pk_mul_f32 v[124:125], v[124:125], v[158:159]
	v_pk_mul_f32 v[122:123], v[122:123], v[156:157]
	v_pk_mul_f32 v[128:129], v[128:129], v[154:155]
	v_pk_mul_f32 v[126:127], v[126:127], v[152:153]
	s_mov_b32 s72, 1.0
	s_mov_b32 s70, 1.0
	s_cbranch_scc1 .LBB0_612
	v_lshl_add_u64 v[156:157], s[48:49], 0, v[150:151]
	v_lshl_add_u64 v[156:157], s[74:75], 1, v[156:157]
	s_lshl_b32 s76, s50, 1
	v_lshl_add_u64 v[156:157], v[156:157], 0, s[76:77]
	v_lshl_add_u64 v[156:157], v[130:131], 1, v[156:157]
	s_mov_b32 s70, 0
	v_cvt_pk_bf16_f32 v152, v122, v123
	v_cvt_pk_bf16_f32 v153, v124, v125
	v_cvt_pk_bf16_f32 v154, v126, v127
	v_cvt_pk_bf16_f32 v155, v128, v129
	global_store_dwordx4 v[156:157], v[152:155], off

;     __device__ __forceinline__ void operator()(AccT& acc, const gm::GUnit& u, int wr, int wc, int fr, int fq) const {
;     ...
;         for (int q = 0; q < 4; ++q) {
;             const int ai = q >> 1, m0 = (q & 1) * 2;
;             u32x2 ga[2][2], gb[2][2];
; #pragma unroll
;             for (int mi = 0; mi < 2; ++mi)
; #pragma unroll
;                 for (int bj = 0; bj < 2; ++bj) {
;                     const unsigned char* gp = gbase + (size_t)(ai * 128 + (m0 + mi) * 16) * INW + bj * 128;
;                     ga[mi][bj] = *(const u32x2*)gp;
;                     gb[mi][bj] = (k < 3) ? *(const u32x2*)(gp + 1024) : (u32x2){0xffffffffu, 0xffffffffu};
;                 }
;             __builtin_amdgcn_sched_barrier(0);
; #pragma unroll
;             for (int mi = 0; mi < 2; ++mi) {
;                 const int m = m0 + mi, row = u.pm * 256 + ai * 128 + wr * 64 + m * 16 + fr;
; #pragma unroll
;                 for (int bj = 0; bj < 2; ++bj) {
;                     const u32x2 a = ga[mi][bj], b = gb[mi][bj];
;                     f32x4 r0, r1;
;                     r0[0] = (float)(a.x & 255u) * __builtin_amdgcn_rcpf((float)(b.x & 255u)); r0[1] = (float)((a.x >> 8) & 255u) * __builtin_amdgcn_rcpf((float)((b.x >> 8) & 255u));
;                     r0[2] = (float)((a.x >> 16) & 255u) * __builtin_amdgcn_rcpf((float)((b.x >> 16) & 255u)); r0[3] = (float)(a.x >> 24) * __builtin_amdgcn_rcpf((float)(b.x >> 24));
;                     r1[0] = (float)(a.y & 255u) * __builtin_amdgcn_rcpf((float)(b.y & 255u)); r1[1] = (float)((a.y >> 8) & 255u) * __builtin_amdgcn_rcpf((float)((b.y >> 8) & 255u));
;                     r1[2] = (float)((a.y >> 16) & 255u) * __builtin_amdgcn_rcpf((float)((b.y >> 16) & 255u)); r1[3] = (float)(a.y >> 24) * __builtin_amdgcn_rcpf((float)(b.y >> 24));
;                     const f32x4 s0 = acc[ai][bj][m][0] * r0, s1 = acc[ai][bj][m][1] * r1;
;                     if (k == 3) {
;                         u32x4 w; w.x = cvt_pk_bf16(s0[0], s0[1]); w.y = cvt_pk_bf16(s0[2], s0[3]); w.z = cvt_pk_bf16(s1[0], s1[1]); w.w = cvt_pk_bf16(s1[2], s1[3]);
;                         *(u32x4*)(M + (size_t)row * DM + u.pn * 256 + bj * 128 + wc * 32 + 8 * fq) = w;
;                     }
;                     const float kz = (k == 3) ? 0.f : 1.f;
;                     acc[ai][bj][m][0] = s0 * kz; acc[ai][bj][m][1] = s1 * kz;
;                 }
.LBB0_618:
	s_nop 1
	s_waitcnt vmcnt(8)
	v_mov_b64_e32 v[152:153], v[166:167]
	v_mov_b64_e32 v[148:149], v[170:171]
	v_mov_b64_e32 v[140:141], v[174:175]
	v_mov_b64_e32 v[138:139], v[178:179]
	s_and_b64 vcc, exec, s[42:43]
	s_cbranch_vccnz .Lmg1_k3
	v_mov_b64_e32 v[154:155], v[168:169]
	v_mov_b64_e32 v[144:145], v[172:173]
	v_mov_b64_e32 v[142:143], v[176:177]
	v_mov_b64_e32 v[136:137], v[192:193]
	s_branch .Lmg1_j
.Lmg1_k3:
	v_mov_b32_e32 v154, -1
	v_mov_b32_e32 v155, -1
	v_mov_b32_e32 v144, -1
	v_mov_b32_e32 v145, -1
	v_mov_b32_e32 v142, -1
	v_mov_b32_e32 v143, -1
	v_mov_b32_e32 v136, -1
	v_mov_b32_e32 v137, -1
.Lmg1_j:
	v_add_co_u32_e32 v234, vcc, 0xa0000, v134
	s_nop 1
	v_addc_co_u32_e32 v235, vcc, 0, v135, vcc
	global_load_dwordx2 v[166:167], v[234:235], off
	global_load_dwordx2 v[168:169], v[234:235], off offset:1024
	global_load_dwordx2 v[170:171], v[234:235], off offset:128
	global_load_dwordx2 v[172:173], v[234:235], off offset:1152
	v_add_co_u32_e32 v234, vcc, 0xb0000, v134
	s_nop 1
	v_addc_co_u32_e32 v235, vcc, 0, v135, vcc
	global_load_dwordx2 v[174:175], v[234:235], off
	global_load_dwordx2 v[176:177], v[234:235], off offset:1024
	global_load_dwordx2 v[178:179], v[234:235], off offset:128
	global_load_dwordx2 v[192:193], v[234:235], off offset:1152
	v_cvt_f32_ubyte0_e32 v133, v154
	v_rcp_iflag_f32_e32 v156, v133
	v_cvt_f32_ubyte1_e32 v133, v154
	v_rcp_iflag_f32_e32 v157, v133
	v_cvt_f32_ubyte2_e32 v133, v154
	v_rcp_iflag_f32_e32 v158, v133
	v_cvt_f32_ubyte3_e32 v133, v154
	v_rcp_iflag_f32_e32 v159, v133
	v_cvt_f32_ubyte3_e32 v161, v152
	v_cvt_f32_ubyte2_e32 v160, v152
	v_cvt_f32_ubyte0_e32 v133, v155
	v_pk_mul_f32 v[158:159], v[158:159], v[160:161]
	v_rcp_iflag_f32_e32 v160, v133
	v_cvt_f32_ubyte1_e32 v133, v155
	v_rcp_iflag_f32_e32 v161, v133
	v_cvt_f32_ubyte2_e32 v133, v155
	v_rcp_iflag_f32_e32 v154, v133
	v_cvt_f32_ubyte3_e32 v133, v155
	v_rcp_iflag_f32_e32 v155, v133
	v_cvt_f32_ubyte1_e32 v163, v152
	v_cvt_f32_ubyte0_e32 v162, v152
	v_add_u32_e32 v150, 32, v132
	v_pk_mul_f32 v[156:157], v[156:157], v[162:163]
	v_cvt_f32_ubyte3_e32 v163, v153
	v_cvt_f32_ubyte2_e32 v162, v153
	v_cvt_f32_ubyte1_e32 v165, v153
	v_cvt_f32_ubyte0_e32 v164, v153
	v_ashrrev_i32_e32 v151, 31, v150
	v_pk_mul_f32 v[152:153], v[160:161], v[164:165]
	v_pk_mul_f32 v[154:155], v[154:155], v[162:163]
	v_lshlrev_b64 v[150:151], 11, v[150:151]
	v_pk_mul_f32 v[92:93], v[92:93], v[158:159]
	v_pk_mul_f32 v[90:91], v[90:91], v[156:157]
	v_pk_mul_f32 v[96:97], v[96:97], v[154:155]
	v_pk_mul_f32 v[94:95], v[94:95], v[152:153]
	s_mov_b32 s84, 1.0
	s_and_b64 vcc, exec, s[40:41]
	s_mov_b32 s82, 1.0
	s_cbranch_vccnz .LBB0_628
	v_lshl_add_u64 v[156:157], s[48:49], 0, v[150:151]
	v_lshl_add_u64 v[156:157], s[74:75], 1, v[156:157]
	s_lshl_b32 s76, s50, 1
	v_lshl_add_u64 v[156:157], v[156:157], 0, s[76:77]
	v_lshl_add_u64 v[156:157], v[130:131], 1, v[156:157]
	s_mov_b32 s82, 0
	v_cvt_pk_bf16_f32 v152, v90, v91
	v_cvt_pk_bf16_f32 v153, v92, v93
	v_cvt_pk_bf16_f32 v154, v94, v95
	v_cvt_pk_bf16_f32 v155, v96, v97
	global_store_dwordx4 v[156:157], v[152:155], off

;     __device__ __forceinline__ void operator()(AccT& acc, const gm::GUnit& u, int wr, int wc, int fr, int fq) const {
;     ...
;         for (int q = 0; q < 4; ++q) {
;             const int ai = q >> 1, m0 = (q & 1) * 2;
;             u32x2 ga[2][2], gb[2][2];
; #pragma unroll
;             for (int mi = 0; mi < 2; ++mi)
; #pragma unroll
;                 for (int bj = 0; bj < 2; ++bj) {
;                     const unsigned char* gp = gbase + (size_t)(ai * 128 + (m0 + mi) * 16) * INW + bj * 128;
;                     ga[mi][bj] = *(const u32x2*)gp;
;                     gb[mi][bj] = (k < 3) ? *(const u32x2*)(gp + 1024) : (u32x2){0xffffffffu, 0xffffffffu};
;                 }
.LBB0_634:
	s_nop 1
	s_waitcnt vmcnt(8)
	v_mov_b64_e32 v[152:153], v[194:195]
	v_mov_b64_e32 v[148:149], v[202:203]
	v_mov_b64_e32 v[140:141], v[206:207]
	v_mov_b64_e32 v[138:139], v[210:211]
	s_and_b64 vcc, exec, s[42:43]
	s_cbranch_vccnz .Lmg2_k3
	v_mov_b64_e32 v[154:155], v[200:201]
	v_mov_b64_e32 v[144:145], v[204:205]
	v_mov_b64_e32 v[142:143], v[208:209]
	v_mov_b64_e32 v[136:137], v[224:225]
	s_branch .Lmg2_j

;     __device__ __forceinline__ void operator()(AccT& acc, const gm::GUnit& u, int wr, int wc, int fr, int fq) const {
;     ...
;         for (int q = 0; q < 4; ++q) {
;             const int ai = q >> 1, m0 = (q & 1) * 2;
;             u32x2 ga[2][2], gb[2][2];
; #pragma unroll
;             for (int mi = 0; mi < 2; ++mi)
; #pragma unroll
;                 for (int bj = 0; bj < 2; ++bj) {
;                     const unsigned char* gp = gbase + (size_t)(ai * 128 + (m0 + mi) * 16) * INW + bj * 128;
;                     ga[mi][bj] = *(const u32x2*)gp;
;                     gb[mi][bj] = (k < 3) ? *(const u32x2*)(gp + 1024) : (u32x2){0xffffffffu, 0xffffffffu};
;                 }
;             __builtin_amdgcn_sched_barrier(0);
; #pragma unroll
;             for (int mi = 0; mi < 2; ++mi) {
;                 const int m = m0 + mi, row = u.pm * 256 + ai * 128 + wr * 64 + m * 16 + fr;
; #pragma unroll
;                 for (int bj = 0; bj < 2; ++bj) {
;                     const u32x2 a = ga[mi][bj], b = gb[mi][bj];
;                     f32x4 r0, r1;
;                     r0[0] = (float)(a.x & 255u) * __builtin_amdgcn_rcpf((float)(b.x & 255u)); r0[1] = (float)((a.x >> 8) & 255u) * __builtin_amdgcn_rcpf((float)((b.x >> 8) & 255u));
;                     r0[2] = (float)((a.x >> 16) & 255u) * __builtin_amdgcn_rcpf((float)((b.x >> 16) & 255u)); r0[3] = (float)(a.x >> 24) * __builtin_amdgcn_rcpf((float)(b.x >> 24));
;                     r1[0] = (float)(a.y & 255u) * __builtin_amdgcn_rcpf((float)(b.y & 255u)); r1[1] = (float)((a.y >> 8) & 255u) * __builtin_amdgcn_rcpf((float)((b.y >> 8) & 255u));
;                     r1[2] = (float)((a.y >> 16) & 255u) * __builtin_amdgcn_rcpf((float)((b.y >> 16) & 255u)); r1[3] = (float)(a.y >> 24) * __builtin_amdgcn_rcpf((float)(b.y >> 24));
;                     const f32x4 s0 = acc[ai][bj][m][0] * r0, s1 = acc[ai][bj][m][1] * r1;
;                     if (k == 3) {
;                         u32x4 w; w.x = cvt_pk_bf16(s0[0], s0[1]); w.y = cvt_pk_bf16(s0[2], s0[3]); w.z = cvt_pk_bf16(s1[0], s1[1]); w.w = cvt_pk_bf16(s1[2], s1[3]);
;                         *(u32x4*)(M + (size_t)row * DM + u.pn * 256 + bj * 128 + wc * 32 + 8 * fq) = w;
;                     }
;                     const float kz = (k == 3) ? 0.f : 1.f;
;                     acc[ai][bj][m][0] = s0 * kz; acc[ai][bj][m][1] = s1 * kz;
;                 }
.Lmg2_j:
	v_cvt_f32_ubyte0_e32 v133, v154
	v_rcp_iflag_f32_e32 v156, v133
	v_cvt_f32_ubyte1_e32 v133, v154
	v_rcp_iflag_f32_e32 v157, v133
	v_cvt_f32_ubyte2_e32 v133, v154
	v_rcp_iflag_f32_e32 v158, v133
	v_cvt_f32_ubyte3_e32 v133, v154
	v_rcp_iflag_f32_e32 v159, v133
	v_cvt_f32_ubyte3_e32 v161, v152
	v_cvt_f32_ubyte2_e32 v160, v152
	v_cvt_f32_ubyte0_e32 v133, v155
	v_pk_mul_f32 v[158:159], v[158:159], v[160:161]
	v_rcp_iflag_f32_e32 v160, v133
	v_cvt_f32_ubyte1_e32 v133, v155
	v_rcp_iflag_f32_e32 v161, v133
	v_cvt_f32_ubyte2_e32 v133, v155
	v_rcp_iflag_f32_e32 v154, v133
	v_cvt_f32_ubyte3_e32 v133, v155
	v_rcp_iflag_f32_e32 v155, v133
	v_cvt_f32_ubyte1_e32 v163, v152
	v_cvt_f32_ubyte0_e32 v162, v152
	v_add_u32_e32 v150, 0x80, v132
	v_pk_mul_f32 v[156:157], v[156:157], v[162:163]
	v_cvt_f32_ubyte3_e32 v163, v153
	v_cvt_f32_ubyte2_e32 v162, v153
	v_cvt_f32_ubyte1_e32 v165, v153
	v_cvt_f32_ubyte0_e32 v164, v153
	v_ashrrev_i32_e32 v151, 31, v150
	v_pk_mul_f32 v[152:153], v[160:161], v[164:165]
	v_pk_mul_f32 v[154:155], v[154:155], v[162:163]
	v_lshlrev_b64 v[150:151], 11, v[150:151]
	v_pk_mul_f32 v[60:61], v[60:61], v[158:159]
	v_pk_mul_f32 v[58:59], v[58:59], v[156:157]
	v_pk_mul_f32 v[64:65], v[64:65], v[154:155]
	v_pk_mul_f32 v[62:63], v[62:63], v[152:153]
	s_mov_b32 s24, 1.0
	s_and_b64 vcc, exec, s[40:41]
	s_mov_b32 s28, 1.0
	s_cbranch_vccnz .LBB0_644
	v_lshl_add_u64 v[156:157], s[48:49], 0, v[150:151]
	v_lshl_add_u64 v[156:157], s[74:75], 1, v[156:157]
	s_lshl_b32 s76, s50, 1
	v_lshl_add_u64 v[156:157], v[156:157], 0, s[76:77]
	v_lshl_add_u64 v[156:157], v[130:131], 1, v[156:157]
	s_mov_b32 s28, 0
	v_cvt_pk_bf16_f32 v152, v58, v59
	v_cvt_pk_bf16_f32 v153, v60, v61
	v_cvt_pk_bf16_f32 v154, v62, v63
	v_cvt_pk_bf16_f32 v155, v64, v65
	global_store_dwordx4 v[156:157], v[152:155], off

;     __device__ __forceinline__ void operator()(AccT& acc, const gm::GUnit& u, int wr, int wc, int fr, int fq) const {
;     ...
;         for (int q = 0; q < 4; ++q) {
;             const int ai = q >> 1, m0 = (q & 1) * 2;
;             u32x2 ga[2][2], gb[2][2];
; #pragma unroll
;             for (int mi = 0; mi < 2; ++mi)
; #pragma unroll
;                 for (int bj = 0; bj < 2; ++bj) {
;                     const unsigned char* gp = gbase + (size_t)(ai * 128 + (m0 + mi) * 16) * INW + bj * 128;
;                     ga[mi][bj] = *(const u32x2*)gp;
;                     gb[mi][bj] = (k < 3) ? *(const u32x2*)(gp + 1024) : (u32x2){0xffffffffu, 0xffffffffu};
;                 }
;             __builtin_amdgcn_sched_barrier(0);
; #pragma unroll
;             for (int mi = 0; mi < 2; ++mi) {
;                 const int m = m0 + mi, row = u.pm * 256 + ai * 128 + wr * 64 + m * 16 + fr;
; #pragma unroll
;                 for (int bj = 0; bj < 2; ++bj) {
;                     const u32x2 a = ga[mi][bj], b = gb[mi][bj];
;                     f32x4 r0, r1;
;                     r0[0] = (float)(a.x & 255u) * __builtin_amdgcn_rcpf((float)(b.x & 255u)); r0[1] = (float)((a.x >> 8) & 255u) * __builtin_amdgcn_rcpf((float)((b.x >> 8) & 255u));
;                     r0[2] = (float)((a.x >> 16) & 255u) * __builtin_amdgcn_rcpf((float)((b.x >> 16) & 255u)); r0[3] = (float)(a.x >> 24) * __builtin_amdgcn_rcpf((float)(b.x >> 24));
;                     r1[0] = (float)(a.y & 255u) * __builtin_amdgcn_rcpf((float)(b.y & 255u)); r1[1] = (float)((a.y >> 8) & 255u) * __builtin_amdgcn_rcpf((float)((b.y >> 8) & 255u));
;                     r1[2] = (float)((a.y >> 16) & 255u) * __builtin_amdgcn_rcpf((float)((b.y >> 16) & 255u)); r1[3] = (float)(a.y >> 24) * __builtin_amdgcn_rcpf((float)(b.y >> 24));
;                     const f32x4 s0 = acc[ai][bj][m][0] * r0, s1 = acc[ai][bj][m][1] * r1;
;                     if (k == 3) {
;                         u32x4 w; w.x = cvt_pk_bf16(s0[0], s0[1]); w.y = cvt_pk_bf16(s0[2], s0[3]); w.z = cvt_pk_bf16(s1[0], s1[1]); w.w = cvt_pk_bf16(s1[2], s1[3]);
;                         *(u32x4*)(M + (size_t)row * DM + u.pn * 256 + bj * 128 + wc * 32 + 8 * fq) = w;
;                     }
;                     const float kz = (k == 3) ? 0.f : 1.f;
;                     acc[ai][bj][m][0] = s0 * kz; acc[ai][bj][m][1] = s1 * kz;
;                 }
.LBB0_650:
	s_nop 1
	s_waitcnt vmcnt(0)
	v_mov_b64_e32 v[150:151], v[166:167]
	v_mov_b64_e32 v[148:149], v[170:171]
	v_mov_b64_e32 v[140:141], v[174:175]
	v_mov_b64_e32 v[138:139], v[178:179]
	s_and_b64 vcc, exec, s[42:43]
	s_cbranch_vccnz .Lmg3_k3
	v_mov_b64_e32 v[152:153], v[168:169]
	v_mov_b64_e32 v[144:145], v[172:173]
	v_mov_b64_e32 v[142:143], v[176:177]
	v_mov_b64_e32 v[136:137], v[192:193]
	s_branch .Lmg3_j
.Lmg3_k3:
	v_mov_b32_e32 v152, -1
	v_mov_b32_e32 v153, -1
	v_mov_b32_e32 v144, -1
	v_mov_b32_e32 v145, -1
	v_mov_b32_e32 v142, -1
	v_mov_b32_e32 v143, -1
	v_mov_b32_e32 v136, -1
	v_mov_b32_e32 v137, -1
.Lmg3_j:
	v_cvt_f32_ubyte0_e32 v133, v152
	v_rcp_iflag_f32_e32 v154, v133
	v_cvt_f32_ubyte1_e32 v133, v152
	v_rcp_iflag_f32_e32 v155, v133
	v_cvt_f32_ubyte2_e32 v133, v152
	v_rcp_iflag_f32_e32 v156, v133
	v_cvt_f32_ubyte3_e32 v133, v152
	v_rcp_iflag_f32_e32 v157, v133
	v_cvt_f32_ubyte3_e32 v159, v150
	v_cvt_f32_ubyte2_e32 v158, v150
	v_cvt_f32_ubyte0_e32 v133, v153
	v_pk_mul_f32 v[156:157], v[156:157], v[158:159]
	v_rcp_iflag_f32_e32 v158, v133
	v_cvt_f32_ubyte1_e32 v133, v153
	v_rcp_iflag_f32_e32 v159, v133
	v_cvt_f32_ubyte2_e32 v133, v153
	v_rcp_iflag_f32_e32 v152, v133
	v_cvt_f32_ubyte3_e32 v133, v153
	v_rcp_iflag_f32_e32 v153, v133
	v_cvt_f32_ubyte1_e32 v161, v150
	v_cvt_f32_ubyte0_e32 v160, v150
	v_add_u32_e32 v134, 0xa0, v132
	v_pk_mul_f32 v[154:155], v[154:155], v[160:161]
	v_cvt_f32_ubyte3_e32 v161, v151
	v_cvt_f32_ubyte2_e32 v160, v151
	v_cvt_f32_ubyte1_e32 v163, v151
	v_cvt_f32_ubyte0_e32 v162, v151
	v_ashrrev_i32_e32 v135, 31, v134
	v_pk_mul_f32 v[150:151], v[158:159], v[162:163]
	v_pk_mul_f32 v[152:153], v[152:153], v[160:161]
	v_lshlrev_b64 v[134:135], 11, v[134:135]
	v_pk_mul_f32 v[28:29], v[28:29], v[156:157]
	v_pk_mul_f32 v[26:27], v[26:27], v[154:155]
	v_pk_mul_f32 v[32:33], v[32:33], v[152:153]
	v_pk_mul_f32 v[30:31], v[30:31], v[150:151]
	s_mov_b32 s22, 1.0
	s_and_b64 vcc, exec, s[40:41]
	s_mov_b32 s42, 1.0
	s_cbranch_vccnz .LBB0_660
	v_lshl_add_u64 v[154:155], s[48:49], 0, v[134:135]
	v_lshl_add_u64 v[154:155], s[74:75], 1, v[154:155]
	s_lshl_b32 s76, s50, 1
	v_lshl_add_u64 v[154:155], v[154:155], 0, s[76:77]
	v_lshl_add_u64 v[154:155], v[130:131], 1, v[154:155]
	s_mov_b32 s42, 0
	v_cvt_pk_bf16_f32 v150, v26, v27
	v_cvt_pk_bf16_f32 v151, v28, v29
	v_cvt_pk_bf16_f32 v152, v30, v31
	v_cvt_pk_bf16_f32 v153, v32, v33
	global_store_dwordx4 v[154:155], v[150:153], off
